# P8 router: serial 32-lane top-k (about 4000 instructions on one half-wave) replaced by a rank-based selection on all 512 threads, 16 lanes x 4 experts per token with DPP row rotations; same ordering a
# speedup vs baseline: 1.0117x; 1.0117x over previous
.LBB0_1230:
	v_add_u32_e32 v2, 0xc400, v177
	ds_write2_b32 v2, v122, v118 offset1:16
	ds_write2_b32 v2, v123, v119 offset0:64 offset1:80
	ds_write2_b32 v2, v124, v120 offset0:128 offset1:144
	ds_write2_b32 v2, v125, v121 offset0:192 offset1:208
	s_nop 0
	ds_write2_b32 v2, v110, v98 offset0:32 offset1:48
	ds_write2_b32 v2, v111, v99 offset0:96 offset1:112
	ds_write2_b32 v2, v112, v100 offset0:160 offset1:176
	ds_write2_b32 v2, v113, v101 offset0:224 offset1:240
	v_add_u32_e32 v2, 0xd400, v177
	ds_write2_b32 v2, v126, v114 offset1:16
	ds_write2_b32 v2, v127, v115 offset0:64 offset1:80
	ds_write2_b32 v2, v128, v116 offset0:128 offset1:144
	ds_write2_b32 v2, v129, v117 offset0:192 offset1:208
	ds_write2_b32 v2, v102, v106 offset0:32 offset1:48
	ds_write2_b32 v2, v103, v107 offset0:96 offset1:112
	ds_write2_b32 v2, v104, v108 offset0:160 offset1:176
	ds_write2_b32 v2, v105, v109 offset0:224 offset1:240
	s_waitcnt lgkmcnt(0)
	s_barrier
	global_load_dwordx4 v[2:5], v[132:133], off
	ds_read_b128 v[6:9], v169 offset:50176
	ds_read_b128 v[10:13], v169 offset:58368
	ds_read_b128 v[14:17], v170 offset:16384
	s_waitcnt lgkmcnt(2)
	v_pk_add_f32 v[8:9], v[8:9], 0 op_sel_hi:[1,0]
	v_pk_add_f32 v[6:7], v[6:7], 0 op_sel_hi:[1,0]
	s_waitcnt vmcnt(12) lgkmcnt(1)
	v_pk_add_f32 v[30:31], v[8:9], v[12:13]
	v_pk_add_f32 v[10:11], v[6:7], v[10:11]
	ds_read_b128 v[6:9], v170 offset:24576
	s_waitcnt lgkmcnt(1)
	v_pk_add_f32 v[14:15], v[10:11], v[14:15]
	ds_read_b128 v[10:13], v170 offset:32768
	ds_read_b128 v[18:21], v170 offset:40960
	ds_read_b128 v[22:25], v170 offset:49152
	ds_read_b128 v[26:29], v170 offset:57344
	s_waitcnt lgkmcnt(4)
	v_pk_add_f32 v[6:7], v[14:15], v[6:7]
	s_waitcnt lgkmcnt(3)
	v_pk_add_f32 v[6:7], v[6:7], v[10:11]
	v_pk_add_f32 v[10:11], v[30:31], v[16:17]
	s_waitcnt lgkmcnt(2)
	v_pk_add_f32 v[6:7], v[6:7], v[18:19]
	v_pk_add_f32 v[8:9], v[10:11], v[8:9]
	s_waitcnt lgkmcnt(1)
	v_pk_add_f32 v[6:7], v[6:7], v[22:23]
	v_pk_add_f32 v[8:9], v[8:9], v[12:13]
	s_waitcnt lgkmcnt(0)
	v_pk_add_f32 v[6:7], v[6:7], v[26:27]
	v_pk_add_f32 v[8:9], v[8:9], v[20:21]
	v_mul_f32_e32 v6, 0xbfb8aa3b, v6
	v_mul_f32_e32 v7, 0xbfb8aa3b, v7
	v_exp_f32_e32 v6, v6
	v_exp_f32_e32 v7, v7
	v_pk_add_f32 v[8:9], v[8:9], v[24:25]
	v_pk_add_f32 v[6:7], v[6:7], 1.0 op_sel_hi:[1,0]
	s_nop 0
	v_div_scale_f32 v10, s[0:1], v7, v7, 1.0
	v_rcp_f32_e32 v11, v10
	v_pk_add_f32 v[8:9], v[8:9], v[28:29]
	v_fma_f32 v12, -v10, v11, 1.0
	v_fmac_f32_e32 v11, v12, v11
	v_div_scale_f32 v12, vcc, 1.0, v7, 1.0
	v_mul_f32_e32 v13, v12, v11
	v_fma_f32 v14, -v10, v13, v12
	v_fmac_f32_e32 v13, v14, v11
	v_fma_f32 v10, -v10, v13, v12
	v_div_scale_f32 v12, s[0:1], v6, v6, 1.0
	v_rcp_f32_e32 v14, v12
	v_div_fmas_f32 v10, v10, v11, v13
	v_mul_f32_e32 v8, 0xbfb8aa3b, v8
	v_mul_f32_e32 v9, 0xbfb8aa3b, v9
	v_div_fixup_f32 v7, v10, v7, 1.0
	v_fma_f32 v10, -v12, v14, 1.0
	v_exp_f32_e32 v8, v8
	v_exp_f32_e32 v9, v9
	v_fmac_f32_e32 v14, v10, v14
	v_div_scale_f32 v10, vcc, 1.0, v6, 1.0
	v_mul_f32_e32 v11, v10, v14
	v_fma_f32 v13, -v12, v11, v10
	v_fmac_f32_e32 v11, v13, v14
	v_pk_add_f32 v[8:9], v[8:9], 1.0 op_sel_hi:[1,0]
	v_fma_f32 v10, -v12, v11, v10
	v_div_scale_f32 v12, s[0:1], v9, v9, 1.0
	v_rcp_f32_e32 v13, v12
	v_div_fmas_f32 v10, v10, v14, v11
	v_div_fixup_f32 v6, v10, v6, 1.0
	v_fma_f32 v10, -v12, v13, 1.0
	v_fmac_f32_e32 v13, v10, v13
	v_div_scale_f32 v10, vcc, 1.0, v9, 1.0
	v_mul_f32_e32 v11, v10, v13
	v_fma_f32 v14, -v12, v11, v10
	v_fmac_f32_e32 v11, v14, v13
	v_fma_f32 v10, -v12, v11, v10
	v_div_scale_f32 v12, s[0:1], v8, v8, 1.0
	v_rcp_f32_e32 v14, v12
	v_div_fmas_f32 v10, v10, v13, v11
	v_div_fixup_f32 v9, v10, v9, 1.0
	s_waitcnt vmcnt(0)
	v_pk_add_f32 v[2:3], v[2:3], v[6:7]
	v_fma_f32 v10, -v12, v14, 1.0
	v_fmac_f32_e32 v14, v10, v14
	v_div_scale_f32 v10, vcc, 1.0, v8, 1.0
	v_mul_f32_e32 v11, v10, v14
	v_fma_f32 v13, -v12, v11, v10
	v_fmac_f32_e32 v11, v13, v14
	v_fma_f32 v10, -v12, v11, v10
	v_div_fmas_f32 v10, v10, v14, v11
	v_div_fixup_f32 v8, v10, v8, 1.0
	v_pk_add_f32 v[4:5], v[8:9], v[4:5]
	ds_write_b128 v171, v[6:9]
	ds_write_b128 v172, v[2:5]
	s_waitcnt lgkmcnt(0)
	s_barrier
	s_mov_b64 s[36:37], exec
	v_and_b32_e32 v10, 15, v0
	v_lshrrev_b32_e32 v11, 1, v10
	v_max_f32_e32 v39, v2, v3
	v_min_f32_e32 v40, v2, v3
	v_max_f32_e32 v41, v4, v5
	v_min_f32_e32 v42, v4, v5
	v_max_f32_e32 v40, v40, v42
	v_min_f32_e32 v42, v39, v41
	v_max_f32_e32 v39, v39, v41
	v_max_f32_e32 v40, v40, v42
	s_nop 0
	v_mov_b32_dpp v41, v39 quad_perm:[1,0,3,2] row_mask:0xf bank_mask:0xf
	v_mov_b32_dpp v42, v40 quad_perm:[1,0,3,2] row_mask:0xf bank_mask:0xf
	v_min_f32_e32 v43, v39, v41
	v_max_f32_e32 v40, v40, v42
	v_max_f32_e32 v39, v39, v41
	v_max_f32_e32 v40, v40, v43
	v_add_f32_e32 v36, v39, v40
	v_ashrrev_i32_e32 v39, 31, v36
	v_or_b32_e32 v39, 0x80000000, v39
	v_xor_b32_e32 v37, v36, v39
	v_mov_b32_e32 v38, 0
	s_nop 0
	v_mov_b32_dpp v39, v37 row_ror:2 row_mask:0xf bank_mask:0xf
	v_mov_b32_dpp v40, v11 row_ror:2 row_mask:0xf bank_mask:0xf
	s_nop 0
	v_cmp_gt_u32_e64 s[0:1], v39, v37
	v_cmp_eq_u32_e64 s[2:3], v39, v37
	v_cmp_lt_u32_e64 s[4:5], v40, v11
	s_and_b64 s[2:3], s[2:3], s[4:5]
	s_or_b64 s[0:1], s[0:1], s[2:3]
	v_addc_co_u32_e64 v38, vcc, 0, v38, s[0:1]
	v_mov_b32_dpp v39, v37 row_ror:4 row_mask:0xf bank_mask:0xf
	v_mov_b32_dpp v40, v11 row_ror:4 row_mask:0xf bank_mask:0xf
	s_nop 0
	v_cmp_gt_u32_e64 s[0:1], v39, v37
	v_cmp_eq_u32_e64 s[2:3], v39, v37
	v_cmp_lt_u32_e64 s[4:5], v40, v11
	s_and_b64 s[2:3], s[2:3], s[4:5]
	s_or_b64 s[0:1], s[0:1], s[2:3]
	v_addc_co_u32_e64 v38, vcc, 0, v38, s[0:1]
	v_mov_b32_dpp v39, v37 row_ror:6 row_mask:0xf bank_mask:0xf
	v_mov_b32_dpp v40, v11 row_ror:6 row_mask:0xf bank_mask:0xf
	s_nop 0
	v_cmp_gt_u32_e64 s[0:1], v39, v37
	v_cmp_eq_u32_e64 s[2:3], v39, v37
	v_cmp_lt_u32_e64 s[4:5], v40, v11
	s_and_b64 s[2:3], s[2:3], s[4:5]
	s_or_b64 s[0:1], s[0:1], s[2:3]
	v_addc_co_u32_e64 v38, vcc, 0, v38, s[0:1]
	v_mov_b32_dpp v39, v37 row_ror:8 row_mask:0xf bank_mask:0xf
	v_mov_b32_dpp v40, v11 row_ror:8 row_mask:0xf bank_mask:0xf
	s_nop 0
	v_cmp_gt_u32_e64 s[0:1], v39, v37
	v_cmp_eq_u32_e64 s[2:3], v39, v37
	v_cmp_lt_u32_e64 s[4:5], v40, v11
	s_and_b64 s[2:3], s[2:3], s[4:5]
	s_or_b64 s[0:1], s[0:1], s[2:3]
	v_addc_co_u32_e64 v38, vcc, 0, v38, s[0:1]
	v_mov_b32_dpp v39, v37 row_ror:10 row_mask:0xf bank_mask:0xf
	v_mov_b32_dpp v40, v11 row_ror:10 row_mask:0xf bank_mask:0xf
	s_nop 0
	v_cmp_gt_u32_e64 s[0:1], v39, v37
	v_cmp_eq_u32_e64 s[2:3], v39, v37
	v_cmp_lt_u32_e64 s[4:5], v40, v11
	s_and_b64 s[2:3], s[2:3], s[4:5]
	s_or_b64 s[0:1], s[0:1], s[2:3]
	v_addc_co_u32_e64 v38, vcc, 0, v38, s[0:1]
	v_mov_b32_dpp v39, v37 row_ror:12 row_mask:0xf bank_mask:0xf
	v_mov_b32_dpp v40, v11 row_ror:12 row_mask:0xf bank_mask:0xf
	s_nop 0
	v_cmp_gt_u32_e64 s[0:1], v39, v37
	v_cmp_eq_u32_e64 s[2:3], v39, v37
	v_cmp_lt_u32_e64 s[4:5], v40, v11
	s_and_b64 s[2:3], s[2:3], s[4:5]
	s_or_b64 s[0:1], s[0:1], s[2:3]
	v_addc_co_u32_e64 v38, vcc, 0, v38, s[0:1]
	v_mov_b32_dpp v39, v37 row_ror:14 row_mask:0xf bank_mask:0xf
	v_mov_b32_dpp v40, v11 row_ror:14 row_mask:0xf bank_mask:0xf
	s_nop 0
	v_cmp_gt_u32_e64 s[0:1], v39, v37
	v_cmp_eq_u32_e64 s[2:3], v39, v37
	v_cmp_lt_u32_e64 s[4:5], v40, v11
	s_and_b64 s[2:3], s[2:3], s[4:5]
	s_or_b64 s[0:1], s[0:1], s[2:3]
	v_addc_co_u32_e64 v38, vcc, 0, v38, s[0:1]
	v_cmp_gt_u32_e64 s[14:15], 4, v38
	v_ashrrev_i32_e32 v24, 31, v2
	v_ashrrev_i32_e32 v25, 31, v3
	v_ashrrev_i32_e32 v26, 31, v4
	v_ashrrev_i32_e32 v27, 31, v5
	v_or_b32_e32 v24, 0x80000000, v24
	v_or_b32_e32 v25, 0x80000000, v25
	v_or_b32_e32 v26, 0x80000000, v26
	v_or_b32_e32 v27, 0x80000000, v27
	v_xor_b32_e32 v20, v2, v24
	v_xor_b32_e32 v21, v3, v25
	v_xor_b32_e32 v22, v4, v26
	v_xor_b32_e32 v23, v5, v27
	v_cndmask_b32_e64 v20, 0, v20, s[14:15]
	v_cndmask_b32_e64 v21, 0, v21, s[14:15]
	v_cndmask_b32_e64 v22, 0, v22, s[14:15]
	v_cndmask_b32_e64 v23, 0, v23, s[14:15]
	v_add_u32_e32 v24, -1, v20
	v_add_u32_e32 v25, -1, v21
	v_add_u32_e32 v26, -1, v22
	v_add_u32_e32 v27, -1, v23
	v_mov_b32_e32 v28, 0
	v_mov_b32_e32 v29, 0
	v_mov_b32_e32 v30, 0
	v_mov_b32_e32 v31, 0
	ds_write_b128 v172, v[20:23]
	v_and_b32_e32 v41, 0xffffff00, v172
	s_waitcnt lgkmcnt(0)
	ds_read_b128 v[44:47], v41
	ds_read_b128 v[48:51], v41 offset:16
	ds_read_b128 v[52:55], v41 offset:32
	ds_read_b128 v[56:59], v41 offset:48
	ds_read_b128 v[200:203], v41 offset:64
	ds_read_b128 v[204:207], v41 offset:80
	ds_read_b128 v[208:211], v41 offset:96
	ds_read_b128 v[212:215], v41 offset:112
	ds_read_b128 v[184:187], v41 offset:128
	ds_read_b128 v[188:191], v41 offset:144
	ds_read_b128 v[220:223], v41 offset:160
	ds_read_b128 v[224:227], v41 offset:176
	ds_read_b128 v[68:71], v41 offset:192
	ds_read_b128 v[248:251], v41 offset:208
	ds_read_b128 v[12:15], v41 offset:224
	ds_read_b128 v[16:19], v41 offset:240
	s_waitcnt lgkmcnt(15)
	v_cmp_gt_u32_e64 s[12:13], v10, 0
	s_nop 1
	v_cndmask_b32_e64 v32, v20, v24, s[12:13]
	v_cndmask_b32_e64 v33, v21, v25, s[12:13]
	v_cndmask_b32_e64 v34, v22, v26, s[12:13]
	v_cndmask_b32_e64 v35, v23, v27, s[12:13]
	v_cmp_gt_u32_e64 s[0:1], v44, v32
	v_cmp_gt_u32_e64 s[2:3], v44, v33
	v_cmp_gt_u32_e64 s[4:5], v44, v34
	v_cmp_gt_u32_e64 s[10:11], v44, v35
	v_addc_co_u32_e64 v28, vcc, 0, v28, s[0:1]
	v_addc_co_u32_e64 v29, vcc, 0, v29, s[2:3]
	v_addc_co_u32_e64 v30, vcc, 0, v30, s[4:5]
	v_addc_co_u32_e64 v31, vcc, 0, v31, s[10:11]
	v_cmp_gt_u32_e64 s[0:1], v45, v32
	v_cmp_gt_u32_e64 s[2:3], v45, v33
	v_cmp_gt_u32_e64 s[4:5], v45, v34
	v_cmp_gt_u32_e64 s[10:11], v45, v35
	v_addc_co_u32_e64 v28, vcc, 0, v28, s[0:1]
	v_addc_co_u32_e64 v29, vcc, 0, v29, s[2:3]
	v_addc_co_u32_e64 v30, vcc, 0, v30, s[4:5]
	v_addc_co_u32_e64 v31, vcc, 0, v31, s[10:11]
	v_cmp_gt_u32_e64 s[0:1], v46, v32
	v_cmp_gt_u32_e64 s[2:3], v46, v33
	v_cmp_gt_u32_e64 s[4:5], v46, v34
	v_cmp_gt_u32_e64 s[10:11], v46, v35
	v_addc_co_u32_e64 v28, vcc, 0, v28, s[0:1]
	v_addc_co_u32_e64 v29, vcc, 0, v29, s[2:3]
	v_addc_co_u32_e64 v30, vcc, 0, v30, s[4:5]
	v_addc_co_u32_e64 v31, vcc, 0, v31, s[10:11]
	v_cmp_gt_u32_e64 s[0:1], v47, v32
	v_cmp_gt_u32_e64 s[2:3], v47, v33
	v_cmp_gt_u32_e64 s[4:5], v47, v34
	v_cmp_gt_u32_e64 s[10:11], v47, v35
	v_addc_co_u32_e64 v28, vcc, 0, v28, s[0:1]
	v_addc_co_u32_e64 v29, vcc, 0, v29, s[2:3]
	v_addc_co_u32_e64 v30, vcc, 0, v30, s[4:5]
	v_addc_co_u32_e64 v31, vcc, 0, v31, s[10:11]
	s_waitcnt lgkmcnt(14)
	v_cmp_gt_u32_e64 s[12:13], v10, 1
	s_nop 1
	v_cndmask_b32_e64 v32, v20, v24, s[12:13]
	v_cndmask_b32_e64 v33, v21, v25, s[12:13]
	v_cndmask_b32_e64 v34, v22, v26, s[12:13]
	v_cndmask_b32_e64 v35, v23, v27, s[12:13]
	v_cmp_gt_u32_e64 s[0:1], v48, v32
	v_cmp_gt_u32_e64 s[2:3], v48, v33
	v_cmp_gt_u32_e64 s[4:5], v48, v34
	v_cmp_gt_u32_e64 s[10:11], v48, v35
	v_addc_co_u32_e64 v28, vcc, 0, v28, s[0:1]
	v_addc_co_u32_e64 v29, vcc, 0, v29, s[2:3]
	v_addc_co_u32_e64 v30, vcc, 0, v30, s[4:5]
	v_addc_co_u32_e64 v31, vcc, 0, v31, s[10:11]
	v_cmp_gt_u32_e64 s[0:1], v49, v32
	v_cmp_gt_u32_e64 s[2:3], v49, v33
	v_cmp_gt_u32_e64 s[4:5], v49, v34
	v_cmp_gt_u32_e64 s[10:11], v49, v35
	v_addc_co_u32_e64 v28, vcc, 0, v28, s[0:1]
	v_addc_co_u32_e64 v29, vcc, 0, v29, s[2:3]
	v_addc_co_u32_e64 v30, vcc, 0, v30, s[4:5]
	v_addc_co_u32_e64 v31, vcc, 0, v31, s[10:11]
	v_cmp_gt_u32_e64 s[0:1], v50, v32
	v_cmp_gt_u32_e64 s[2:3], v50, v33
	v_cmp_gt_u32_e64 s[4:5], v50, v34
	v_cmp_gt_u32_e64 s[10:11], v50, v35
	v_addc_co_u32_e64 v28, vcc, 0, v28, s[0:1]
	v_addc_co_u32_e64 v29, vcc, 0, v29, s[2:3]
	v_addc_co_u32_e64 v30, vcc, 0, v30, s[4:5]
	v_addc_co_u32_e64 v31, vcc, 0, v31, s[10:11]
	v_cmp_gt_u32_e64 s[0:1], v51, v32
	v_cmp_gt_u32_e64 s[2:3], v51, v33
	v_cmp_gt_u32_e64 s[4:5], v51, v34
	v_cmp_gt_u32_e64 s[10:11], v51, v35
	v_addc_co_u32_e64 v28, vcc, 0, v28, s[0:1]
	v_addc_co_u32_e64 v29, vcc, 0, v29, s[2:3]
	v_addc_co_u32_e64 v30, vcc, 0, v30, s[4:5]
	v_addc_co_u32_e64 v31, vcc, 0, v31, s[10:11]
	s_waitcnt lgkmcnt(13)
	v_cmp_gt_u32_e64 s[12:13], v10, 2
	s_nop 1
	v_cndmask_b32_e64 v32, v20, v24, s[12:13]
	v_cndmask_b32_e64 v33, v21, v25, s[12:13]
	v_cndmask_b32_e64 v34, v22, v26, s[12:13]
	v_cndmask_b32_e64 v35, v23, v27, s[12:13]
	v_cmp_gt_u32_e64 s[0:1], v52, v32
	v_cmp_gt_u32_e64 s[2:3], v52, v33
	v_cmp_gt_u32_e64 s[4:5], v52, v34
	v_cmp_gt_u32_e64 s[10:11], v52, v35
	v_addc_co_u32_e64 v28, vcc, 0, v28, s[0:1]
	v_addc_co_u32_e64 v29, vcc, 0, v29, s[2:3]
	v_addc_co_u32_e64 v30, vcc, 0, v30, s[4:5]
	v_addc_co_u32_e64 v31, vcc, 0, v31, s[10:11]
	v_cmp_gt_u32_e64 s[0:1], v53, v32
	v_cmp_gt_u32_e64 s[2:3], v53, v33
	v_cmp_gt_u32_e64 s[4:5], v53, v34
	v_cmp_gt_u32_e64 s[10:11], v53, v35
	v_addc_co_u32_e64 v28, vcc, 0, v28, s[0:1]
	v_addc_co_u32_e64 v29, vcc, 0, v29, s[2:3]
	v_addc_co_u32_e64 v30, vcc, 0, v30, s[4:5]
	v_addc_co_u32_e64 v31, vcc, 0, v31, s[10:11]
	v_cmp_gt_u32_e64 s[0:1], v54, v32
	v_cmp_gt_u32_e64 s[2:3], v54, v33
	v_cmp_gt_u32_e64 s[4:5], v54, v34
	v_cmp_gt_u32_e64 s[10:11], v54, v35
	v_addc_co_u32_e64 v28, vcc, 0, v28, s[0:1]
	v_addc_co_u32_e64 v29, vcc, 0, v29, s[2:3]
	v_addc_co_u32_e64 v30, vcc, 0, v30, s[4:5]
	v_addc_co_u32_e64 v31, vcc, 0, v31, s[10:11]
	v_cmp_gt_u32_e64 s[0:1], v55, v32
	v_cmp_gt_u32_e64 s[2:3], v55, v33
	v_cmp_gt_u32_e64 s[4:5], v55, v34
	v_cmp_gt_u32_e64 s[10:11], v55, v35
	v_addc_co_u32_e64 v28, vcc, 0, v28, s[0:1]
	v_addc_co_u32_e64 v29, vcc, 0, v29, s[2:3]
	v_addc_co_u32_e64 v30, vcc, 0, v30, s[4:5]
	v_addc_co_u32_e64 v31, vcc, 0, v31, s[10:11]
	s_waitcnt lgkmcnt(12)
	v_cmp_gt_u32_e64 s[12:13], v10, 3
	s_nop 1
	v_cndmask_b32_e64 v32, v20, v24, s[12:13]
	v_cndmask_b32_e64 v33, v21, v25, s[12:13]
	v_cndmask_b32_e64 v34, v22, v26, s[12:13]
	v_cndmask_b32_e64 v35, v23, v27, s[12:13]
	v_cmp_gt_u32_e64 s[0:1], v56, v32
	v_cmp_gt_u32_e64 s[2:3], v56, v33
	v_cmp_gt_u32_e64 s[4:5], v56, v34
	v_cmp_gt_u32_e64 s[10:11], v56, v35
	v_addc_co_u32_e64 v28, vcc, 0, v28, s[0:1]
	v_addc_co_u32_e64 v29, vcc, 0, v29, s[2:3]
	v_addc_co_u32_e64 v30, vcc, 0, v30, s[4:5]
	v_addc_co_u32_e64 v31, vcc, 0, v31, s[10:11]
	v_cmp_gt_u32_e64 s[0:1], v57, v32
	v_cmp_gt_u32_e64 s[2:3], v57, v33
	v_cmp_gt_u32_e64 s[4:5], v57, v34
	v_cmp_gt_u32_e64 s[10:11], v57, v35
	v_addc_co_u32_e64 v28, vcc, 0, v28, s[0:1]
	v_addc_co_u32_e64 v29, vcc, 0, v29, s[2:3]
	v_addc_co_u32_e64 v30, vcc, 0, v30, s[4:5]
	v_addc_co_u32_e64 v31, vcc, 0, v31, s[10:11]
	v_cmp_gt_u32_e64 s[0:1], v58, v32
	v_cmp_gt_u32_e64 s[2:3], v58, v33
	v_cmp_gt_u32_e64 s[4:5], v58, v34
	v_cmp_gt_u32_e64 s[10:11], v58, v35
	v_addc_co_u32_e64 v28, vcc, 0, v28, s[0:1]
	v_addc_co_u32_e64 v29, vcc, 0, v29, s[2:3]
	v_addc_co_u32_e64 v30, vcc, 0, v30, s[4:5]
	v_addc_co_u32_e64 v31, vcc, 0, v31, s[10:11]
	v_cmp_gt_u32_e64 s[0:1], v59, v32
	v_cmp_gt_u32_e64 s[2:3], v59, v33
	v_cmp_gt_u32_e64 s[4:5], v59, v34
	v_cmp_gt_u32_e64 s[10:11], v59, v35
	v_addc_co_u32_e64 v28, vcc, 0, v28, s[0:1]
	v_addc_co_u32_e64 v29, vcc, 0, v29, s[2:3]
	v_addc_co_u32_e64 v30, vcc, 0, v30, s[4:5]
	v_addc_co_u32_e64 v31, vcc, 0, v31, s[10:11]
	s_waitcnt lgkmcnt(11)
	v_cmp_gt_u32_e64 s[12:13], v10, 4
	s_nop 1
	v_cndmask_b32_e64 v32, v20, v24, s[12:13]
	v_cndmask_b32_e64 v33, v21, v25, s[12:13]
	v_cndmask_b32_e64 v34, v22, v26, s[12:13]
	v_cndmask_b32_e64 v35, v23, v27, s[12:13]
	v_cmp_gt_u32_e64 s[0:1], v200, v32
	v_cmp_gt_u32_e64 s[2:3], v200, v33
	v_cmp_gt_u32_e64 s[4:5], v200, v34
	v_cmp_gt_u32_e64 s[10:11], v200, v35
	v_addc_co_u32_e64 v28, vcc, 0, v28, s[0:1]
	v_addc_co_u32_e64 v29, vcc, 0, v29, s[2:3]
	v_addc_co_u32_e64 v30, vcc, 0, v30, s[4:5]
	v_addc_co_u32_e64 v31, vcc, 0, v31, s[10:11]
	v_cmp_gt_u32_e64 s[0:1], v201, v32
	v_cmp_gt_u32_e64 s[2:3], v201, v33
	v_cmp_gt_u32_e64 s[4:5], v201, v34
	v_cmp_gt_u32_e64 s[10:11], v201, v35
	v_addc_co_u32_e64 v28, vcc, 0, v28, s[0:1]
	v_addc_co_u32_e64 v29, vcc, 0, v29, s[2:3]
	v_addc_co_u32_e64 v30, vcc, 0, v30, s[4:5]
	v_addc_co_u32_e64 v31, vcc, 0, v31, s[10:11]
	v_cmp_gt_u32_e64 s[0:1], v202, v32
	v_cmp_gt_u32_e64 s[2:3], v202, v33
	v_cmp_gt_u32_e64 s[4:5], v202, v34
	v_cmp_gt_u32_e64 s[10:11], v202, v35
	v_addc_co_u32_e64 v28, vcc, 0, v28, s[0:1]
	v_addc_co_u32_e64 v29, vcc, 0, v29, s[2:3]
	v_addc_co_u32_e64 v30, vcc, 0, v30, s[4:5]
	v_addc_co_u32_e64 v31, vcc, 0, v31, s[10:11]
	v_cmp_gt_u32_e64 s[0:1], v203, v32
	v_cmp_gt_u32_e64 s[2:3], v203, v33
	v_cmp_gt_u32_e64 s[4:5], v203, v34
	v_cmp_gt_u32_e64 s[10:11], v203, v35
	v_addc_co_u32_e64 v28, vcc, 0, v28, s[0:1]
	v_addc_co_u32_e64 v29, vcc, 0, v29, s[2:3]
	v_addc_co_u32_e64 v30, vcc, 0, v30, s[4:5]
	v_addc_co_u32_e64 v31, vcc, 0, v31, s[10:11]
	s_waitcnt lgkmcnt(10)
	v_cmp_gt_u32_e64 s[12:13], v10, 5
	s_nop 1
	v_cndmask_b32_e64 v32, v20, v24, s[12:13]
	v_cndmask_b32_e64 v33, v21, v25, s[12:13]
	v_cndmask_b32_e64 v34, v22, v26, s[12:13]
	v_cndmask_b32_e64 v35, v23, v27, s[12:13]
	v_cmp_gt_u32_e64 s[0:1], v204, v32
	v_cmp_gt_u32_e64 s[2:3], v204, v33
	v_cmp_gt_u32_e64 s[4:5], v204, v34
	v_cmp_gt_u32_e64 s[10:11], v204, v35
	v_addc_co_u32_e64 v28, vcc, 0, v28, s[0:1]
	v_addc_co_u32_e64 v29, vcc, 0, v29, s[2:3]
	v_addc_co_u32_e64 v30, vcc, 0, v30, s[4:5]
	v_addc_co_u32_e64 v31, vcc, 0, v31, s[10:11]
	v_cmp_gt_u32_e64 s[0:1], v205, v32
	v_cmp_gt_u32_e64 s[2:3], v205, v33
	v_cmp_gt_u32_e64 s[4:5], v205, v34
	v_cmp_gt_u32_e64 s[10:11], v205, v35
	v_addc_co_u32_e64 v28, vcc, 0, v28, s[0:1]
	v_addc_co_u32_e64 v29, vcc, 0, v29, s[2:3]
	v_addc_co_u32_e64 v30, vcc, 0, v30, s[4:5]
	v_addc_co_u32_e64 v31, vcc, 0, v31, s[10:11]
	v_cmp_gt_u32_e64 s[0:1], v206, v32
	v_cmp_gt_u32_e64 s[2:3], v206, v33
	v_cmp_gt_u32_e64 s[4:5], v206, v34
	v_cmp_gt_u32_e64 s[10:11], v206, v35
	v_addc_co_u32_e64 v28, vcc, 0, v28, s[0:1]
	v_addc_co_u32_e64 v29, vcc, 0, v29, s[2:3]
	v_addc_co_u32_e64 v30, vcc, 0, v30, s[4:5]
	v_addc_co_u32_e64 v31, vcc, 0, v31, s[10:11]
	v_cmp_gt_u32_e64 s[0:1], v207, v32
	v_cmp_gt_u32_e64 s[2:3], v207, v33
	v_cmp_gt_u32_e64 s[4:5], v207, v34
	v_cmp_gt_u32_e64 s[10:11], v207, v35
	v_addc_co_u32_e64 v28, vcc, 0, v28, s[0:1]
	v_addc_co_u32_e64 v29, vcc, 0, v29, s[2:3]
	v_addc_co_u32_e64 v30, vcc, 0, v30, s[4:5]
	v_addc_co_u32_e64 v31, vcc, 0, v31, s[10:11]
	s_waitcnt lgkmcnt(9)
	v_cmp_gt_u32_e64 s[12:13], v10, 6
	s_nop 1
	v_cndmask_b32_e64 v32, v20, v24, s[12:13]
	v_cndmask_b32_e64 v33, v21, v25, s[12:13]
	v_cndmask_b32_e64 v34, v22, v26, s[12:13]
	v_cndmask_b32_e64 v35, v23, v27, s[12:13]
	v_cmp_gt_u32_e64 s[0:1], v208, v32
	v_cmp_gt_u32_e64 s[2:3], v208, v33
	v_cmp_gt_u32_e64 s[4:5], v208, v34
	v_cmp_gt_u32_e64 s[10:11], v208, v35
	v_addc_co_u32_e64 v28, vcc, 0, v28, s[0:1]
	v_addc_co_u32_e64 v29, vcc, 0, v29, s[2:3]
	v_addc_co_u32_e64 v30, vcc, 0, v30, s[4:5]
	v_addc_co_u32_e64 v31, vcc, 0, v31, s[10:11]
	v_cmp_gt_u32_e64 s[0:1], v209, v32
	v_cmp_gt_u32_e64 s[2:3], v209, v33
	v_cmp_gt_u32_e64 s[4:5], v209, v34
	v_cmp_gt_u32_e64 s[10:11], v209, v35
	v_addc_co_u32_e64 v28, vcc, 0, v28, s[0:1]
	v_addc_co_u32_e64 v29, vcc, 0, v29, s[2:3]
	v_addc_co_u32_e64 v30, vcc, 0, v30, s[4:5]
	v_addc_co_u32_e64 v31, vcc, 0, v31, s[10:11]
	v_cmp_gt_u32_e64 s[0:1], v210, v32
	v_cmp_gt_u32_e64 s[2:3], v210, v33
	v_cmp_gt_u32_e64 s[4:5], v210, v34
	v_cmp_gt_u32_e64 s[10:11], v210, v35
	v_addc_co_u32_e64 v28, vcc, 0, v28, s[0:1]
	v_addc_co_u32_e64 v29, vcc, 0, v29, s[2:3]
	v_addc_co_u32_e64 v30, vcc, 0, v30, s[4:5]
	v_addc_co_u32_e64 v31, vcc, 0, v31, s[10:11]
	v_cmp_gt_u32_e64 s[0:1], v211, v32
	v_cmp_gt_u32_e64 s[2:3], v211, v33
	v_cmp_gt_u32_e64 s[4:5], v211, v34
	v_cmp_gt_u32_e64 s[10:11], v211, v35
	v_addc_co_u32_e64 v28, vcc, 0, v28, s[0:1]
	v_addc_co_u32_e64 v29, vcc, 0, v29, s[2:3]
	v_addc_co_u32_e64 v30, vcc, 0, v30, s[4:5]
	v_addc_co_u32_e64 v31, vcc, 0, v31, s[10:11]
	s_waitcnt lgkmcnt(8)
	v_cmp_gt_u32_e64 s[12:13], v10, 7
	s_nop 1
	v_cndmask_b32_e64 v32, v20, v24, s[12:13]
	v_cndmask_b32_e64 v33, v21, v25, s[12:13]
	v_cndmask_b32_e64 v34, v22, v26, s[12:13]
	v_cndmask_b32_e64 v35, v23, v27, s[12:13]
	v_cmp_gt_u32_e64 s[0:1], v212, v32
	v_cmp_gt_u32_e64 s[2:3], v212, v33
	v_cmp_gt_u32_e64 s[4:5], v212, v34
	v_cmp_gt_u32_e64 s[10:11], v212, v35
	v_addc_co_u32_e64 v28, vcc, 0, v28, s[0:1]
	v_addc_co_u32_e64 v29, vcc, 0, v29, s[2:3]
	v_addc_co_u32_e64 v30, vcc, 0, v30, s[4:5]
	v_addc_co_u32_e64 v31, vcc, 0, v31, s[10:11]
	v_cmp_gt_u32_e64 s[0:1], v213, v32
	v_cmp_gt_u32_e64 s[2:3], v213, v33
	v_cmp_gt_u32_e64 s[4:5], v213, v34
	v_cmp_gt_u32_e64 s[10:11], v213, v35
	v_addc_co_u32_e64 v28, vcc, 0, v28, s[0:1]
	v_addc_co_u32_e64 v29, vcc, 0, v29, s[2:3]
	v_addc_co_u32_e64 v30, vcc, 0, v30, s[4:5]
	v_addc_co_u32_e64 v31, vcc, 0, v31, s[10:11]
	v_cmp_gt_u32_e64 s[0:1], v214, v32
	v_cmp_gt_u32_e64 s[2:3], v214, v33
	v_cmp_gt_u32_e64 s[4:5], v214, v34
	v_cmp_gt_u32_e64 s[10:11], v214, v35
	v_addc_co_u32_e64 v28, vcc, 0, v28, s[0:1]
	v_addc_co_u32_e64 v29, vcc, 0, v29, s[2:3]
	v_addc_co_u32_e64 v30, vcc, 0, v30, s[4:5]
	v_addc_co_u32_e64 v31, vcc, 0, v31, s[10:11]
	v_cmp_gt_u32_e64 s[0:1], v215, v32
	v_cmp_gt_u32_e64 s[2:3], v215, v33
	v_cmp_gt_u32_e64 s[4:5], v215, v34
	v_cmp_gt_u32_e64 s[10:11], v215, v35
	v_addc_co_u32_e64 v28, vcc, 0, v28, s[0:1]
	v_addc_co_u32_e64 v29, vcc, 0, v29, s[2:3]
	v_addc_co_u32_e64 v30, vcc, 0, v30, s[4:5]
	v_addc_co_u32_e64 v31, vcc, 0, v31, s[10:11]
	s_waitcnt lgkmcnt(7)
	v_cmp_gt_u32_e64 s[12:13], v10, 8
	s_nop 1
	v_cndmask_b32_e64 v32, v20, v24, s[12:13]
	v_cndmask_b32_e64 v33, v21, v25, s[12:13]
	v_cndmask_b32_e64 v34, v22, v26, s[12:13]
	v_cndmask_b32_e64 v35, v23, v27, s[12:13]
	v_cmp_gt_u32_e64 s[0:1], v184, v32
	v_cmp_gt_u32_e64 s[2:3], v184, v33
	v_cmp_gt_u32_e64 s[4:5], v184, v34
	v_cmp_gt_u32_e64 s[10:11], v184, v35
	v_addc_co_u32_e64 v28, vcc, 0, v28, s[0:1]
	v_addc_co_u32_e64 v29, vcc, 0, v29, s[2:3]
	v_addc_co_u32_e64 v30, vcc, 0, v30, s[4:5]
	v_addc_co_u32_e64 v31, vcc, 0, v31, s[10:11]
	v_cmp_gt_u32_e64 s[0:1], v185, v32
	v_cmp_gt_u32_e64 s[2:3], v185, v33
	v_cmp_gt_u32_e64 s[4:5], v185, v34
	v_cmp_gt_u32_e64 s[10:11], v185, v35
	v_addc_co_u32_e64 v28, vcc, 0, v28, s[0:1]
	v_addc_co_u32_e64 v29, vcc, 0, v29, s[2:3]
	v_addc_co_u32_e64 v30, vcc, 0, v30, s[4:5]
	v_addc_co_u32_e64 v31, vcc, 0, v31, s[10:11]
	v_cmp_gt_u32_e64 s[0:1], v186, v32
	v_cmp_gt_u32_e64 s[2:3], v186, v33
	v_cmp_gt_u32_e64 s[4:5], v186, v34
	v_cmp_gt_u32_e64 s[10:11], v186, v35
	v_addc_co_u32_e64 v28, vcc, 0, v28, s[0:1]
	v_addc_co_u32_e64 v29, vcc, 0, v29, s[2:3]
	v_addc_co_u32_e64 v30, vcc, 0, v30, s[4:5]
	v_addc_co_u32_e64 v31, vcc, 0, v31, s[10:11]
	v_cmp_gt_u32_e64 s[0:1], v187, v32
	v_cmp_gt_u32_e64 s[2:3], v187, v33
	v_cmp_gt_u32_e64 s[4:5], v187, v34
	v_cmp_gt_u32_e64 s[10:11], v187, v35
	v_addc_co_u32_e64 v28, vcc, 0, v28, s[0:1]
	v_addc_co_u32_e64 v29, vcc, 0, v29, s[2:3]
	v_addc_co_u32_e64 v30, vcc, 0, v30, s[4:5]
	v_addc_co_u32_e64 v31, vcc, 0, v31, s[10:11]
	s_waitcnt lgkmcnt(6)
	v_cmp_gt_u32_e64 s[12:13], v10, 9
	s_nop 1
	v_cndmask_b32_e64 v32, v20, v24, s[12:13]
	v_cndmask_b32_e64 v33, v21, v25, s[12:13]
	v_cndmask_b32_e64 v34, v22, v26, s[12:13]
	v_cndmask_b32_e64 v35, v23, v27, s[12:13]
	v_cmp_gt_u32_e64 s[0:1], v188, v32
	v_cmp_gt_u32_e64 s[2:3], v188, v33
	v_cmp_gt_u32_e64 s[4:5], v188, v34
	v_cmp_gt_u32_e64 s[10:11], v188, v35
	v_addc_co_u32_e64 v28, vcc, 0, v28, s[0:1]
	v_addc_co_u32_e64 v29, vcc, 0, v29, s[2:3]
	v_addc_co_u32_e64 v30, vcc, 0, v30, s[4:5]
	v_addc_co_u32_e64 v31, vcc, 0, v31, s[10:11]
	v_cmp_gt_u32_e64 s[0:1], v189, v32
	v_cmp_gt_u32_e64 s[2:3], v189, v33
	v_cmp_gt_u32_e64 s[4:5], v189, v34
	v_cmp_gt_u32_e64 s[10:11], v189, v35
	v_addc_co_u32_e64 v28, vcc, 0, v28, s[0:1]
	v_addc_co_u32_e64 v29, vcc, 0, v29, s[2:3]
	v_addc_co_u32_e64 v30, vcc, 0, v30, s[4:5]
	v_addc_co_u32_e64 v31, vcc, 0, v31, s[10:11]
	v_cmp_gt_u32_e64 s[0:1], v190, v32
	v_cmp_gt_u32_e64 s[2:3], v190, v33
	v_cmp_gt_u32_e64 s[4:5], v190, v34
	v_cmp_gt_u32_e64 s[10:11], v190, v35
	v_addc_co_u32_e64 v28, vcc, 0, v28, s[0:1]
	v_addc_co_u32_e64 v29, vcc, 0, v29, s[2:3]
	v_addc_co_u32_e64 v30, vcc, 0, v30, s[4:5]
	v_addc_co_u32_e64 v31, vcc, 0, v31, s[10:11]
	v_cmp_gt_u32_e64 s[0:1], v191, v32
	v_cmp_gt_u32_e64 s[2:3], v191, v33
	v_cmp_gt_u32_e64 s[4:5], v191, v34
	v_cmp_gt_u32_e64 s[10:11], v191, v35
	v_addc_co_u32_e64 v28, vcc, 0, v28, s[0:1]
	v_addc_co_u32_e64 v29, vcc, 0, v29, s[2:3]
	v_addc_co_u32_e64 v30, vcc, 0, v30, s[4:5]
	v_addc_co_u32_e64 v31, vcc, 0, v31, s[10:11]
	s_waitcnt lgkmcnt(5)
	v_cmp_gt_u32_e64 s[12:13], v10, 10
	s_nop 1
	v_cndmask_b32_e64 v32, v20, v24, s[12:13]
	v_cndmask_b32_e64 v33, v21, v25, s[12:13]
	v_cndmask_b32_e64 v34, v22, v26, s[12:13]
	v_cndmask_b32_e64 v35, v23, v27, s[12:13]
	v_cmp_gt_u32_e64 s[0:1], v220, v32
	v_cmp_gt_u32_e64 s[2:3], v220, v33
	v_cmp_gt_u32_e64 s[4:5], v220, v34
	v_cmp_gt_u32_e64 s[10:11], v220, v35
	v_addc_co_u32_e64 v28, vcc, 0, v28, s[0:1]
	v_addc_co_u32_e64 v29, vcc, 0, v29, s[2:3]
	v_addc_co_u32_e64 v30, vcc, 0, v30, s[4:5]
	v_addc_co_u32_e64 v31, vcc, 0, v31, s[10:11]
	v_cmp_gt_u32_e64 s[0:1], v221, v32
	v_cmp_gt_u32_e64 s[2:3], v221, v33
	v_cmp_gt_u32_e64 s[4:5], v221, v34
	v_cmp_gt_u32_e64 s[10:11], v221, v35
	v_addc_co_u32_e64 v28, vcc, 0, v28, s[0:1]
	v_addc_co_u32_e64 v29, vcc, 0, v29, s[2:3]
	v_addc_co_u32_e64 v30, vcc, 0, v30, s[4:5]
	v_addc_co_u32_e64 v31, vcc, 0, v31, s[10:11]
	v_cmp_gt_u32_e64 s[0:1], v222, v32
	v_cmp_gt_u32_e64 s[2:3], v222, v33
	v_cmp_gt_u32_e64 s[4:5], v222, v34
	v_cmp_gt_u32_e64 s[10:11], v222, v35
	v_addc_co_u32_e64 v28, vcc, 0, v28, s[0:1]
	v_addc_co_u32_e64 v29, vcc, 0, v29, s[2:3]
	v_addc_co_u32_e64 v30, vcc, 0, v30, s[4:5]
	v_addc_co_u32_e64 v31, vcc, 0, v31, s[10:11]
	v_cmp_gt_u32_e64 s[0:1], v223, v32
	v_cmp_gt_u32_e64 s[2:3], v223, v33
	v_cmp_gt_u32_e64 s[4:5], v223, v34
	v_cmp_gt_u32_e64 s[10:11], v223, v35
	v_addc_co_u32_e64 v28, vcc, 0, v28, s[0:1]
	v_addc_co_u32_e64 v29, vcc, 0, v29, s[2:3]
	v_addc_co_u32_e64 v30, vcc, 0, v30, s[4:5]
	v_addc_co_u32_e64 v31, vcc, 0, v31, s[10:11]
	s_waitcnt lgkmcnt(4)
	v_cmp_gt_u32_e64 s[12:13], v10, 11
	s_nop 1
	v_cndmask_b32_e64 v32, v20, v24, s[12:13]
	v_cndmask_b32_e64 v33, v21, v25, s[12:13]
	v_cndmask_b32_e64 v34, v22, v26, s[12:13]
	v_cndmask_b32_e64 v35, v23, v27, s[12:13]
	v_cmp_gt_u32_e64 s[0:1], v224, v32
	v_cmp_gt_u32_e64 s[2:3], v224, v33
	v_cmp_gt_u32_e64 s[4:5], v224, v34
	v_cmp_gt_u32_e64 s[10:11], v224, v35
	v_addc_co_u32_e64 v28, vcc, 0, v28, s[0:1]
	v_addc_co_u32_e64 v29, vcc, 0, v29, s[2:3]
	v_addc_co_u32_e64 v30, vcc, 0, v30, s[4:5]
	v_addc_co_u32_e64 v31, vcc, 0, v31, s[10:11]
	v_cmp_gt_u32_e64 s[0:1], v225, v32
	v_cmp_gt_u32_e64 s[2:3], v225, v33
	v_cmp_gt_u32_e64 s[4:5], v225, v34
	v_cmp_gt_u32_e64 s[10:11], v225, v35
	v_addc_co_u32_e64 v28, vcc, 0, v28, s[0:1]
	v_addc_co_u32_e64 v29, vcc, 0, v29, s[2:3]
	v_addc_co_u32_e64 v30, vcc, 0, v30, s[4:5]
	v_addc_co_u32_e64 v31, vcc, 0, v31, s[10:11]
	v_cmp_gt_u32_e64 s[0:1], v226, v32
	v_cmp_gt_u32_e64 s[2:3], v226, v33
	v_cmp_gt_u32_e64 s[4:5], v226, v34
	v_cmp_gt_u32_e64 s[10:11], v226, v35
	v_addc_co_u32_e64 v28, vcc, 0, v28, s[0:1]
	v_addc_co_u32_e64 v29, vcc, 0, v29, s[2:3]
	v_addc_co_u32_e64 v30, vcc, 0, v30, s[4:5]
	v_addc_co_u32_e64 v31, vcc, 0, v31, s[10:11]
	v_cmp_gt_u32_e64 s[0:1], v227, v32
	v_cmp_gt_u32_e64 s[2:3], v227, v33
	v_cmp_gt_u32_e64 s[4:5], v227, v34
	v_cmp_gt_u32_e64 s[10:11], v227, v35
	v_addc_co_u32_e64 v28, vcc, 0, v28, s[0:1]
	v_addc_co_u32_e64 v29, vcc, 0, v29, s[2:3]
	v_addc_co_u32_e64 v30, vcc, 0, v30, s[4:5]
	v_addc_co_u32_e64 v31, vcc, 0, v31, s[10:11]
	s_waitcnt lgkmcnt(3)
	v_cmp_gt_u32_e64 s[12:13], v10, 12
	s_nop 1
	v_cndmask_b32_e64 v32, v20, v24, s[12:13]
	v_cndmask_b32_e64 v33, v21, v25, s[12:13]
	v_cndmask_b32_e64 v34, v22, v26, s[12:13]
	v_cndmask_b32_e64 v35, v23, v27, s[12:13]
	v_cmp_gt_u32_e64 s[0:1], v68, v32
	v_cmp_gt_u32_e64 s[2:3], v68, v33
	v_cmp_gt_u32_e64 s[4:5], v68, v34
	v_cmp_gt_u32_e64 s[10:11], v68, v35
	v_addc_co_u32_e64 v28, vcc, 0, v28, s[0:1]
	v_addc_co_u32_e64 v29, vcc, 0, v29, s[2:3]
	v_addc_co_u32_e64 v30, vcc, 0, v30, s[4:5]
	v_addc_co_u32_e64 v31, vcc, 0, v31, s[10:11]
	v_cmp_gt_u32_e64 s[0:1], v69, v32
	v_cmp_gt_u32_e64 s[2:3], v69, v33
	v_cmp_gt_u32_e64 s[4:5], v69, v34
	v_cmp_gt_u32_e64 s[10:11], v69, v35
	v_addc_co_u32_e64 v28, vcc, 0, v28, s[0:1]
	v_addc_co_u32_e64 v29, vcc, 0, v29, s[2:3]
	v_addc_co_u32_e64 v30, vcc, 0, v30, s[4:5]
	v_addc_co_u32_e64 v31, vcc, 0, v31, s[10:11]
	v_cmp_gt_u32_e64 s[0:1], v70, v32
	v_cmp_gt_u32_e64 s[2:3], v70, v33
	v_cmp_gt_u32_e64 s[4:5], v70, v34
	v_cmp_gt_u32_e64 s[10:11], v70, v35
	v_addc_co_u32_e64 v28, vcc, 0, v28, s[0:1]
	v_addc_co_u32_e64 v29, vcc, 0, v29, s[2:3]
	v_addc_co_u32_e64 v30, vcc, 0, v30, s[4:5]
	v_addc_co_u32_e64 v31, vcc, 0, v31, s[10:11]
	v_cmp_gt_u32_e64 s[0:1], v71, v32
	v_cmp_gt_u32_e64 s[2:3], v71, v33
	v_cmp_gt_u32_e64 s[4:5], v71, v34
	v_cmp_gt_u32_e64 s[10:11], v71, v35
	v_addc_co_u32_e64 v28, vcc, 0, v28, s[0:1]
	v_addc_co_u32_e64 v29, vcc, 0, v29, s[2:3]
	v_addc_co_u32_e64 v30, vcc, 0, v30, s[4:5]
	v_addc_co_u32_e64 v31, vcc, 0, v31, s[10:11]
	s_waitcnt lgkmcnt(2)
	v_cmp_gt_u32_e64 s[12:13], v10, 13
	s_nop 1
	v_cndmask_b32_e64 v32, v20, v24, s[12:13]
	v_cndmask_b32_e64 v33, v21, v25, s[12:13]
	v_cndmask_b32_e64 v34, v22, v26, s[12:13]
	v_cndmask_b32_e64 v35, v23, v27, s[12:13]
	v_cmp_gt_u32_e64 s[0:1], v248, v32
	v_cmp_gt_u32_e64 s[2:3], v248, v33
	v_cmp_gt_u32_e64 s[4:5], v248, v34
	v_cmp_gt_u32_e64 s[10:11], v248, v35
	v_addc_co_u32_e64 v28, vcc, 0, v28, s[0:1]
	v_addc_co_u32_e64 v29, vcc, 0, v29, s[2:3]
	v_addc_co_u32_e64 v30, vcc, 0, v30, s[4:5]
	v_addc_co_u32_e64 v31, vcc, 0, v31, s[10:11]
	v_cmp_gt_u32_e64 s[0:1], v249, v32
	v_cmp_gt_u32_e64 s[2:3], v249, v33
	v_cmp_gt_u32_e64 s[4:5], v249, v34
	v_cmp_gt_u32_e64 s[10:11], v249, v35
	v_addc_co_u32_e64 v28, vcc, 0, v28, s[0:1]
	v_addc_co_u32_e64 v29, vcc, 0, v29, s[2:3]
	v_addc_co_u32_e64 v30, vcc, 0, v30, s[4:5]
	v_addc_co_u32_e64 v31, vcc, 0, v31, s[10:11]
	v_cmp_gt_u32_e64 s[0:1], v250, v32
	v_cmp_gt_u32_e64 s[2:3], v250, v33
	v_cmp_gt_u32_e64 s[4:5], v250, v34
	v_cmp_gt_u32_e64 s[10:11], v250, v35
	v_addc_co_u32_e64 v28, vcc, 0, v28, s[0:1]
	v_addc_co_u32_e64 v29, vcc, 0, v29, s[2:3]
	v_addc_co_u32_e64 v30, vcc, 0, v30, s[4:5]
	v_addc_co_u32_e64 v31, vcc, 0, v31, s[10:11]
	v_cmp_gt_u32_e64 s[0:1], v251, v32
	v_cmp_gt_u32_e64 s[2:3], v251, v33
	v_cmp_gt_u32_e64 s[4:5], v251, v34
	v_cmp_gt_u32_e64 s[10:11], v251, v35
	v_addc_co_u32_e64 v28, vcc, 0, v28, s[0:1]
	v_addc_co_u32_e64 v29, vcc, 0, v29, s[2:3]
	v_addc_co_u32_e64 v30, vcc, 0, v30, s[4:5]
	v_addc_co_u32_e64 v31, vcc, 0, v31, s[10:11]
	s_waitcnt lgkmcnt(1)
	v_cmp_gt_u32_e64 s[12:13], v10, 14
	s_nop 1
	v_cndmask_b32_e64 v32, v20, v24, s[12:13]
	v_cndmask_b32_e64 v33, v21, v25, s[12:13]
	v_cndmask_b32_e64 v34, v22, v26, s[12:13]
	v_cndmask_b32_e64 v35, v23, v27, s[12:13]
	v_cmp_gt_u32_e64 s[0:1], v12, v32
	v_cmp_gt_u32_e64 s[2:3], v12, v33
	v_cmp_gt_u32_e64 s[4:5], v12, v34
	v_cmp_gt_u32_e64 s[10:11], v12, v35
	v_addc_co_u32_e64 v28, vcc, 0, v28, s[0:1]
	v_addc_co_u32_e64 v29, vcc, 0, v29, s[2:3]
	v_addc_co_u32_e64 v30, vcc, 0, v30, s[4:5]
	v_addc_co_u32_e64 v31, vcc, 0, v31, s[10:11]
	v_cmp_gt_u32_e64 s[0:1], v13, v32
	v_cmp_gt_u32_e64 s[2:3], v13, v33
	v_cmp_gt_u32_e64 s[4:5], v13, v34
	v_cmp_gt_u32_e64 s[10:11], v13, v35
	v_addc_co_u32_e64 v28, vcc, 0, v28, s[0:1]
	v_addc_co_u32_e64 v29, vcc, 0, v29, s[2:3]
	v_addc_co_u32_e64 v30, vcc, 0, v30, s[4:5]
	v_addc_co_u32_e64 v31, vcc, 0, v31, s[10:11]
	v_cmp_gt_u32_e64 s[0:1], v14, v32
	v_cmp_gt_u32_e64 s[2:3], v14, v33
	v_cmp_gt_u32_e64 s[4:5], v14, v34
	v_cmp_gt_u32_e64 s[10:11], v14, v35
	v_addc_co_u32_e64 v28, vcc, 0, v28, s[0:1]
	v_addc_co_u32_e64 v29, vcc, 0, v29, s[2:3]
	v_addc_co_u32_e64 v30, vcc, 0, v30, s[4:5]
	v_addc_co_u32_e64 v31, vcc, 0, v31, s[10:11]
	v_cmp_gt_u32_e64 s[0:1], v15, v32
	v_cmp_gt_u32_e64 s[2:3], v15, v33
	v_cmp_gt_u32_e64 s[4:5], v15, v34
	v_cmp_gt_u32_e64 s[10:11], v15, v35
	v_addc_co_u32_e64 v28, vcc, 0, v28, s[0:1]
	v_addc_co_u32_e64 v29, vcc, 0, v29, s[2:3]
	v_addc_co_u32_e64 v30, vcc, 0, v30, s[4:5]
	v_addc_co_u32_e64 v31, vcc, 0, v31, s[10:11]
	s_waitcnt lgkmcnt(0)
	v_cmp_gt_u32_e64 s[12:13], v10, 15
	s_nop 1
	v_cndmask_b32_e64 v32, v20, v24, s[12:13]
	v_cndmask_b32_e64 v33, v21, v25, s[12:13]
	v_cndmask_b32_e64 v34, v22, v26, s[12:13]
	v_cndmask_b32_e64 v35, v23, v27, s[12:13]
	v_cmp_gt_u32_e64 s[0:1], v16, v32
	v_cmp_gt_u32_e64 s[2:3], v16, v33
	v_cmp_gt_u32_e64 s[4:5], v16, v34
	v_cmp_gt_u32_e64 s[10:11], v16, v35
	v_addc_co_u32_e64 v28, vcc, 0, v28, s[0:1]
	v_addc_co_u32_e64 v29, vcc, 0, v29, s[2:3]
	v_addc_co_u32_e64 v30, vcc, 0, v30, s[4:5]
	v_addc_co_u32_e64 v31, vcc, 0, v31, s[10:11]
	v_cmp_gt_u32_e64 s[0:1], v17, v32
	v_cmp_gt_u32_e64 s[2:3], v17, v33
	v_cmp_gt_u32_e64 s[4:5], v17, v34
	v_cmp_gt_u32_e64 s[10:11], v17, v35
	v_addc_co_u32_e64 v28, vcc, 0, v28, s[0:1]
	v_addc_co_u32_e64 v29, vcc, 0, v29, s[2:3]
	v_addc_co_u32_e64 v30, vcc, 0, v30, s[4:5]
	v_addc_co_u32_e64 v31, vcc, 0, v31, s[10:11]
	v_cmp_gt_u32_e64 s[0:1], v18, v32
	v_cmp_gt_u32_e64 s[2:3], v18, v33
	v_cmp_gt_u32_e64 s[4:5], v18, v34
	v_cmp_gt_u32_e64 s[10:11], v18, v35
	v_addc_co_u32_e64 v28, vcc, 0, v28, s[0:1]
	v_addc_co_u32_e64 v29, vcc, 0, v29, s[2:3]
	v_addc_co_u32_e64 v30, vcc, 0, v30, s[4:5]
	v_addc_co_u32_e64 v31, vcc, 0, v31, s[10:11]
	v_cmp_gt_u32_e64 s[0:1], v19, v32
	v_cmp_gt_u32_e64 s[2:3], v19, v33
	v_cmp_gt_u32_e64 s[4:5], v19, v34
	v_cmp_gt_u32_e64 s[10:11], v19, v35
	v_addc_co_u32_e64 v28, vcc, 0, v28, s[0:1]
	v_addc_co_u32_e64 v29, vcc, 0, v29, s[2:3]
	v_addc_co_u32_e64 v30, vcc, 0, v30, s[4:5]
	v_addc_co_u32_e64 v31, vcc, 0, v31, s[10:11]
	v_cmp_eq_u32_e64 s[0:1], v21, v20
	v_cmp_eq_u32_e64 s[2:3], v22, v20
	v_cmp_eq_u32_e64 s[4:5], v22, v21
	s_nop 0
	v_addc_co_u32_e64 v29, vcc, 0, v29, s[0:1]
	v_addc_co_u32_e64 v30, vcc, 0, v30, s[2:3]
	v_addc_co_u32_e64 v30, vcc, 0, v30, s[4:5]
	v_cmp_eq_u32_e64 s[0:1], v23, v20
	v_cmp_eq_u32_e64 s[2:3], v23, v21
	v_cmp_eq_u32_e64 s[4:5], v23, v22
	s_nop 0
	v_addc_co_u32_e64 v31, vcc, 0, v31, s[0:1]
	v_addc_co_u32_e64 v31, vcc, 0, v31, s[2:3]
	v_addc_co_u32_e64 v31, vcc, 0, v31, s[4:5]
	v_cmp_gt_u32_e64 s[0:1], 8, v28
	v_cmp_gt_u32_e64 s[2:3], 8, v29
	v_cmp_gt_u32_e64 s[4:5], 8, v30
	v_cmp_gt_u32_e64 s[10:11], 8, v31
	s_and_b64 s[0:1], s[0:1], s[14:15]
	s_and_b64 s[2:3], s[2:3], s[14:15]
	s_and_b64 s[4:5], s[4:5], s[14:15]
	s_and_b64 s[10:11], s[10:11], s[14:15]
	v_cndmask_b32_e64 v39, 0, v6, s[0:1]
	v_cndmask_b32_e64 v40, 0, v7, s[2:3]
	v_add_f32_e32 v39, v39, v40
	v_cndmask_b32_e64 v40, 0, v8, s[4:5]
	v_add_f32_e32 v39, v39, v40
	v_cndmask_b32_e64 v40, 0, v9, s[10:11]
	v_add_f32_e32 v39, v39, v40
	s_nop 1
	v_add_f32_dpp v39, v39, v39 row_ror:8 row_mask:0xf bank_mask:0xf
	s_nop 1
	v_add_f32_dpp v39, v39, v39 row_ror:4 row_mask:0xf bank_mask:0xf
	s_nop 1
	v_add_f32_dpp v39, v39, v39 row_ror:2 row_mask:0xf bank_mask:0xf
	s_nop 1
	v_add_f32_dpp v39, v39, v39 row_ror:1 row_mask:0xf bank_mask:0xf
	s_nop 1
	v_rcp_f32_e32 v39, v39
	v_lshrrev_b32_e32 v42, 4, v0
	v_mul_f32_e32 v39, s53, v39
	v_or_b32_e32 v42, s55, v42
	v_lshlrev_b32_e32 v42, 3, v42
	s_mov_b64 exec, s[0:1]
	s_cbranch_execz .Ltopk_skip0
	v_lshl_or_b32 v40, v10, 2, 0
	v_lshl_add_u32 v41, v40, 2, s38
	ds_add_rtn_u32 v43, v41, v178
	v_add_lshl_u32 v41, v42, v28, 2
	v_mul_f32_e32 v32, v6, v39
	global_store_dword v41, v40, s[22:23]
	global_store_dword v41, v32, s[26:27]
	s_waitcnt lgkmcnt(0)
	global_store_dword v41, v43, s[24:25]
.Ltopk_skip0:
	s_mov_b64 exec, s[36:37]
	s_mov_b64 exec, s[2:3]
	s_cbranch_execz .Ltopk_skip1
	v_lshl_or_b32 v40, v10, 2, 1
	v_lshl_add_u32 v41, v40, 2, s38
	ds_add_rtn_u32 v43, v41, v178
	v_add_lshl_u32 v41, v42, v29, 2
	v_mul_f32_e32 v33, v7, v39
	global_store_dword v41, v40, s[22:23]
	global_store_dword v41, v33, s[26:27]
	s_waitcnt lgkmcnt(0)
	global_store_dword v41, v43, s[24:25]
.Ltopk_skip1:
	s_mov_b64 exec, s[36:37]
	s_mov_b64 exec, s[4:5]
	s_cbranch_execz .Ltopk_skip2
	v_lshl_or_b32 v40, v10, 2, 2
	v_lshl_add_u32 v41, v40, 2, s38
	ds_add_rtn_u32 v43, v41, v178
	v_add_lshl_u32 v41, v42, v30, 2
	v_mul_f32_e32 v34, v8, v39
	global_store_dword v41, v40, s[22:23]
	global_store_dword v41, v34, s[26:27]
	s_waitcnt lgkmcnt(0)
	global_store_dword v41, v43, s[24:25]
.Ltopk_skip2:
	s_mov_b64 exec, s[36:37]
	s_mov_b64 exec, s[10:11]
	s_cbranch_execz .Ltopk_skip3
	v_lshl_or_b32 v40, v10, 2, 3
	v_lshl_add_u32 v41, v40, 2, s38
	ds_add_rtn_u32 v43, v41, v178
	v_add_lshl_u32 v41, v42, v31, 2
	v_mul_f32_e32 v35, v9, v39
	global_store_dword v41, v40, s[22:23]
	global_store_dword v41, v35, s[26:27]
	s_waitcnt lgkmcnt(0)
	global_store_dword v41, v43, s[24:25]
.Ltopk_skip3:
	s_mov_b64 exec, s[36:37]
